# SwiGLU epilogue: the two constant multiplies of the sigmoid exponent argument folded into one
# speedup vs baseline: 1.0222x; 1.0026x over previous
.LBB0_1094:
	v_mov_b32_e32 v18, v188
	s_nop 15
	s_nop 15
	s_lshl_b32 s31, s36, 7
	v_readfirstlane_b32 s30, v18
	s_lshr_b32 s36, s30, 1
	s_and_b32 s36, s36, 0x60
	s_or_b32 s31, s36, s31
	v_lshrrev_b32_e32 v0, 1, v18
	v_ashrrev_i32_e32 v167, 31, v166
	v_and_or_b32 v16, v0, 24, s31
	v_lshlrev_b64 v[0:1], 13, v[166:167]
	v_lshl_add_u64 v[0:1], s[28:29], 0, v[0:1]
	v_ashrrev_i32_e32 v17, 31, v16
	v_lshl_add_u64 v[8:9], v[16:17], 2, v[0:1]
	global_load_dwordx4 v[0:3], v[8:9], off offset:16
	global_load_dwordx4 v[4:7], v[8:9], off
	s_movk_i32 s31, 0x1000
	v_lshl_add_u64 v[10:11], v[8:9], 0, s[84:85]
	v_add_co_u32_e32 v8, vcc, s31, v8
	s_ashr_i32 s30, s30, 2
	s_nop 0
	v_addc_co_u32_e32 v9, vcc, 0, v9, vcc
	global_load_dwordx4 v[12:15], v[8:9], off
	s_nop 0
	global_load_dwordx4 v[8:11], v[10:11], off offset:16
	v_lshlrev_b32_e32 v19, 8, v219
	s_andn2_b32 s30, s30, 63
	v_add_u32_e32 v19, s30, v19
	v_and_or_b32 v18, v18, 15, v19
	v_ashrrev_i32_e32 v19, 31, v18
	v_readlane_b32 s30, v254, 30
	v_lshlrev_b64 v[18:19], 10, v[18:19]
	v_readlane_b32 s31, v254, 31
	s_mov_b32 s21, 0x24000
	s_mov_b64 s[40:41], -1
	v_lshl_add_u64 v[18:19], s[30:31], 0, v[18:19]
	v_lshl_add_u64 v[16:17], v[18:19], 0, v[16:17]
	s_mov_b32 s30, 0xc000
	s_mov_b64 s[72:73], 0x400
	v_readlane_b32 s70, v255, 14
	s_mov_b32 s71, s66
	s_waitcnt vmcnt(0)
	v_add_f32_e32 v18, v158, v4
	v_min_f32_e32 v18, 0x40e00000, v18
	v_mul_f32_e32 v20, 0xc01d265f, v18
	v_exp_f32_e32 v20, v20
	v_add_f32_e32 v12, 1.0, v12
	v_add_f32_e32 v20, 1.0, v20
	v_rcp_f32_e32 v20, v20
	v_add_f32_e32 v19, v154, v12
	v_med3_f32 v19, v19, s61, v214
	v_add_f32_e32 v8, 1.0, v8
	v_mul_f32_e32 v18, v18, v20
	v_mul_f32_e32 v18, v19, v18
	v_add_f32_e32 v19, v150, v0
	v_min_f32_e32 v19, 0x40e00000, v19
	v_mul_f32_e32 v21, 0xc01d265f, v19
	v_exp_f32_e32 v21, v21
	v_add_f32_e32 v20, v146, v8
	v_med3_f32 v20, v20, s61, v214
	v_add_f32_e32 v13, 1.0, v13
	v_add_f32_e32 v21, 1.0, v21
	v_rcp_f32_e32 v21, v21
	v_add_f32_e32 v9, 1.0, v9
	v_add_f32_e32 v14, 1.0, v14
	v_add_f32_e32 v10, 1.0, v10
	v_mul_f32_e32 v19, v19, v21
	v_mul_f32_e32 v19, v20, v19
	v_add_f32_e32 v20, v159, v5
	v_min_f32_e32 v20, 0x40e00000, v20
	v_mul_f32_e32 v22, 0xc01d265f, v20
	v_exp_f32_e32 v22, v22
	v_add_f32_e32 v21, v155, v13
	v_med3_f32 v21, v21, s61, v214
	v_add_f32_e32 v15, 1.0, v15
	v_add_f32_e32 v22, 1.0, v22
	v_rcp_f32_e32 v22, v22
	v_add_f32_e32 v11, 1.0, v11
	v_mul_f32_e32 v20, v20, v22
	v_mul_f32_e32 v20, v21, v20
	v_add_f32_e32 v21, v151, v1
	v_min_f32_e32 v21, 0x40e00000, v21
	v_mul_f32_e32 v23, 0xc01d265f, v21
	v_exp_f32_e32 v23, v23
	v_add_f32_e32 v22, v147, v9
	v_med3_f32 v22, v22, s61, v214
	v_add_f32_e32 v23, 1.0, v23
	v_rcp_f32_e32 v23, v23
	s_nop 0
	v_mul_f32_e32 v21, v21, v23
	v_mul_f32_e32 v21, v22, v21
	v_add_f32_e32 v22, v160, v6
	v_min_f32_e32 v22, 0x40e00000, v22
	v_mul_f32_e32 v24, 0xc01d265f, v22
	v_exp_f32_e32 v24, v24
	v_add_f32_e32 v23, v156, v14
	v_med3_f32 v23, v23, s61, v214
	v_add_f32_e32 v24, 1.0, v24
	v_rcp_f32_e32 v24, v24
	s_nop 0
	v_mul_f32_e32 v22, v22, v24
	v_mul_f32_e32 v23, v23, v22
	v_add_f32_e32 v22, v152, v2
	v_min_f32_e32 v22, 0x40e00000, v22
	v_mul_f32_e32 v25, 0xc01d265f, v22
	v_exp_f32_e32 v25, v25
	v_add_f32_e32 v24, v148, v10
	v_med3_f32 v24, v24, s61, v214
	v_add_f32_e32 v25, 1.0, v25
	v_rcp_f32_e32 v25, v25
	s_nop 0
	v_mul_f32_e32 v22, v22, v25
	v_mul_f32_e32 v24, v24, v22
	v_add_f32_e32 v22, v161, v7
	v_min_f32_e32 v22, 0x40e00000, v22
	v_mul_f32_e32 v26, 0xc01d265f, v22
	v_exp_f32_e32 v26, v26
	v_add_f32_e32 v25, v157, v15
	v_med3_f32 v25, v25, s61, v214
	v_add_f32_e32 v26, 1.0, v26
	v_rcp_f32_e32 v26, v26
	s_nop 0
	v_mul_f32_e32 v22, v22, v26
	v_mul_f32_e32 v25, v25, v22
	v_add_f32_e32 v22, v153, v3
	v_min_f32_e32 v22, 0x40e00000, v22
	v_mul_f32_e32 v27, 0xc01d265f, v22
	v_exp_f32_e32 v27, v27
	v_add_f32_e32 v26, v149, v11
	v_med3_f32 v26, v26, s61, v214
	v_add_f32_e32 v27, 1.0, v27
	v_rcp_f32_e32 v27, v27
	s_nop 0
	v_mul_f32_e32 v22, v22, v27
	v_mul_f32_e32 v26, v26, v22
	v_mov_b32_e32 v22, v113
	v_cvt_pk_fp8_f32 v22, v18, v20
	v_add_f32_e32 v18, v142, v4
	v_min_f32_e32 v18, 0x40e00000, v18
	v_mul_f32_e32 v20, 0xc01d265f, v18
	v_exp_f32_e32 v20, v20
	v_cvt_pk_fp8_f32 v22, v23, v25 op_sel:[0,0,1]
	v_mov_b32_e32 v23, v113
	v_cvt_pk_fp8_f32 v23, v19, v21
	v_add_f32_e32 v20, 1.0, v20
	v_rcp_f32_e32 v20, v20
	v_add_f32_e32 v19, v138, v12
	v_med3_f32 v19, v19, s61, v214
	v_cvt_pk_fp8_f32 v23, v24, v26 op_sel:[0,0,1]
	v_mul_f32_e32 v18, v18, v20
	v_mul_f32_e32 v19, v19, v18
	v_add_f32_e32 v18, v134, v0
	v_min_f32_e32 v18, 0x40e00000, v18
	v_mul_f32_e32 v21, 0xc01d265f, v18
	v_exp_f32_e32 v21, v21
	v_add_f32_e32 v20, v130, v8
	v_med3_f32 v20, v20, s61, v214
	global_store_dwordx2 v[16:17], v[22:23], off
	v_add_f32_e32 v21, 1.0, v21
	v_rcp_f32_e32 v21, v21
	s_nop 0
	v_mul_f32_e32 v18, v18, v21
	v_mul_f32_e32 v20, v20, v18
	v_add_f32_e32 v18, v143, v5
	v_min_f32_e32 v18, 0x40e00000, v18
	v_mul_f32_e32 v22, 0xc01d265f, v18
	v_exp_f32_e32 v22, v22
	v_add_f32_e32 v21, v139, v13
	v_med3_f32 v21, v21, s61, v214
	v_add_f32_e32 v22, 1.0, v22
	v_rcp_f32_e32 v22, v22
	s_nop 0
	v_mul_f32_e32 v18, v18, v22
	v_mul_f32_e32 v21, v21, v18
	v_add_f32_e32 v18, v135, v1
	v_min_f32_e32 v18, 0x40e00000, v18
	v_mul_f32_e32 v23, 0xc01d265f, v18
	v_exp_f32_e32 v23, v23
	v_add_f32_e32 v22, v131, v9
	v_med3_f32 v22, v22, s61, v214
	v_add_f32_e32 v23, 1.0, v23
	v_rcp_f32_e32 v23, v23
	s_nop 0
	v_mul_f32_e32 v18, v18, v23
	v_mul_f32_e32 v22, v22, v18
	v_add_f32_e32 v18, v144, v6
	v_min_f32_e32 v18, 0x40e00000, v18
	v_mul_f32_e32 v24, 0xc01d265f, v18
	v_exp_f32_e32 v24, v24
	v_add_f32_e32 v23, v140, v14
	v_med3_f32 v23, v23, s61, v214
	v_add_f32_e32 v24, 1.0, v24
	v_rcp_f32_e32 v24, v24
	s_nop 0
	v_mul_f32_e32 v18, v18, v24
	v_mul_f32_e32 v23, v23, v18
	v_add_f32_e32 v18, v136, v2
	v_min_f32_e32 v18, 0x40e00000, v18
	v_mul_f32_e32 v25, 0xc01d265f, v18
	v_exp_f32_e32 v25, v25
	v_add_f32_e32 v24, v132, v10
	v_med3_f32 v24, v24, s61, v214
	v_add_f32_e32 v25, 1.0, v25
	v_rcp_f32_e32 v25, v25
	s_nop 0
	v_mul_f32_e32 v18, v18, v25
	v_mul_f32_e32 v24, v24, v18
	v_add_f32_e32 v18, v145, v7
	v_min_f32_e32 v18, 0x40e00000, v18
	v_mul_f32_e32 v26, 0xc01d265f, v18
	v_exp_f32_e32 v26, v26
	v_add_f32_e32 v25, v141, v15
	v_med3_f32 v25, v25, s61, v214
	v_add_f32_e32 v26, 1.0, v26
	v_rcp_f32_e32 v26, v26
	s_nop 0
	v_mul_f32_e32 v18, v18, v26
	v_mul_f32_e32 v25, v25, v18
	v_add_f32_e32 v18, v137, v3
	v_min_f32_e32 v18, 0x40e00000, v18
	v_mul_f32_e32 v27, 0xc01d265f, v18
	v_exp_f32_e32 v27, v27
	v_add_f32_e32 v26, v133, v11
	v_med3_f32 v26, v26, s61, v214
	v_add_f32_e32 v27, 1.0, v27
	v_rcp_f32_e32 v27, v27
	s_nop 0
	v_mul_f32_e32 v18, v18, v27
	v_mul_f32_e32 v26, v26, v18
	v_mov_b32_e32 v18, v113
	v_cvt_pk_fp8_f32 v18, v19, v21
	v_mov_b32_e32 v19, v113
	v_cvt_pk_fp8_f32 v19, v20, v22
	v_add_co_u32_e32 v20, vcc, s62, v16
	v_cvt_pk_fp8_f32 v18, v23, v25 op_sel:[0,0,1]
	v_cvt_pk_fp8_f32 v19, v24, v26 op_sel:[0,0,1]
	v_addc_co_u32_e32 v21, vcc, 0, v17, vcc
	global_store_dwordx2 v[20:21], v[18:19], off
	v_add_f32_e32 v18, v126, v4
	v_min_f32_e32 v18, 0x40e00000, v18
	v_mul_f32_e32 v20, 0xc01d265f, v18
	v_exp_f32_e32 v20, v20
	v_add_f32_e32 v19, v122, v12
	v_med3_f32 v19, v19, s61, v214
	v_add_f32_e32 v20, 1.0, v20
	v_rcp_f32_e32 v20, v20
	s_nop 0
	v_mul_f32_e32 v18, v18, v20
	v_mul_f32_e32 v19, v19, v18
	v_add_f32_e32 v18, v118, v0
	v_min_f32_e32 v18, 0x40e00000, v18
	v_mul_f32_e32 v21, 0xc01d265f, v18
	v_exp_f32_e32 v21, v21
	v_add_f32_e32 v20, v114, v8
	v_med3_f32 v20, v20, s61, v214
	v_add_f32_e32 v21, 1.0, v21
	v_rcp_f32_e32 v21, v21
	s_nop 0
	v_mul_f32_e32 v18, v18, v21
	v_mul_f32_e32 v20, v20, v18
	v_add_f32_e32 v18, v127, v5
	v_min_f32_e32 v18, 0x40e00000, v18
	v_mul_f32_e32 v22, 0xc01d265f, v18
	v_exp_f32_e32 v22, v22
	v_add_f32_e32 v21, v123, v13
	v_med3_f32 v21, v21, s61, v214
	v_add_f32_e32 v22, 1.0, v22
	v_rcp_f32_e32 v22, v22
	s_nop 0
	v_mul_f32_e32 v18, v18, v22
	v_mul_f32_e32 v21, v21, v18
	v_add_f32_e32 v18, v119, v1
	v_min_f32_e32 v18, 0x40e00000, v18
	v_mul_f32_e32 v23, 0xc01d265f, v18
	v_exp_f32_e32 v23, v23
	v_add_f32_e32 v22, v115, v9
	v_med3_f32 v22, v22, s61, v214
	v_add_f32_e32 v23, 1.0, v23
	v_rcp_f32_e32 v23, v23
	s_nop 0
	v_mul_f32_e32 v18, v18, v23
	v_mul_f32_e32 v22, v22, v18
	v_add_f32_e32 v18, v128, v6
	v_min_f32_e32 v18, 0x40e00000, v18
	v_mul_f32_e32 v24, 0xc01d265f, v18
	v_exp_f32_e32 v24, v24
	v_add_f32_e32 v23, v124, v14
	v_med3_f32 v23, v23, s61, v214
	v_add_f32_e32 v24, 1.0, v24
	v_rcp_f32_e32 v24, v24
	s_nop 0
	v_mul_f32_e32 v18, v18, v24
	v_mul_f32_e32 v23, v23, v18
	v_add_f32_e32 v18, v120, v2
	v_min_f32_e32 v18, 0x40e00000, v18
	v_mul_f32_e32 v25, 0xc01d265f, v18
	v_exp_f32_e32 v25, v25
	v_add_f32_e32 v24, v116, v10
	v_med3_f32 v24, v24, s61, v214
	v_add_f32_e32 v25, 1.0, v25
	v_rcp_f32_e32 v25, v25
	s_nop 0
	v_mul_f32_e32 v18, v18, v25
	v_mul_f32_e32 v24, v24, v18
	v_add_f32_e32 v18, v129, v7
	v_min_f32_e32 v18, 0x40e00000, v18
	v_mul_f32_e32 v26, 0xc01d265f, v18
	v_exp_f32_e32 v26, v26
	v_add_f32_e32 v25, v125, v15
	v_med3_f32 v25, v25, s61, v214
	v_add_f32_e32 v26, 1.0, v26
	v_rcp_f32_e32 v26, v26
	s_nop 0
	v_mul_f32_e32 v18, v18, v26
	v_mul_f32_e32 v25, v25, v18
	v_add_f32_e32 v18, v121, v3
	v_min_f32_e32 v18, 0x40e00000, v18
	v_mul_f32_e32 v27, 0xc01d265f, v18
	v_exp_f32_e32 v27, v27
	v_add_f32_e32 v26, v117, v11
	v_med3_f32 v26, v26, s61, v214
	v_add_f32_e32 v27, 1.0, v27
	v_rcp_f32_e32 v27, v27
	s_nop 0
	v_mul_f32_e32 v18, v18, v27
	v_mul_f32_e32 v26, v26, v18
	v_mov_b32_e32 v18, v113
	v_cvt_pk_fp8_f32 v18, v19, v21
	v_mov_b32_e32 v19, v113
	v_cvt_pk_fp8_f32 v19, v20, v22
	v_add_co_u32_e32 v20, vcc, s24, v16
	v_cvt_pk_fp8_f32 v18, v23, v25 op_sel:[0,0,1]
	v_cvt_pk_fp8_f32 v19, v24, v26 op_sel:[0,0,1]
	v_addc_co_u32_e32 v21, vcc, 0, v17, vcc
	global_store_dwordx2 v[20:21], v[18:19], off
	v_add_f32_e32 v18, v108, v4
	v_min_f32_e32 v18, 0x40e00000, v18
	v_mul_f32_e32 v20, 0xc01d265f, v18
	v_exp_f32_e32 v20, v20
	v_add_f32_e32 v19, v104, v12
	v_med3_f32 v19, v19, s61, v214
	v_add_f32_e32 v20, 1.0, v20
	v_rcp_f32_e32 v20, v20
	s_nop 0
	v_mul_f32_e32 v18, v18, v20
	v_mul_f32_e32 v19, v19, v18
	v_add_f32_e32 v18, v100, v0
	v_min_f32_e32 v18, 0x40e00000, v18
	v_mul_f32_e32 v21, 0xc01d265f, v18
	v_exp_f32_e32 v21, v21
	v_add_f32_e32 v20, v96, v8
	v_med3_f32 v20, v20, s61, v214
	v_add_f32_e32 v21, 1.0, v21
	v_rcp_f32_e32 v21, v21
	s_nop 0
	v_mul_f32_e32 v18, v18, v21
	v_mul_f32_e32 v20, v20, v18
	v_add_f32_e32 v18, v109, v5
	v_min_f32_e32 v18, 0x40e00000, v18
	v_mul_f32_e32 v22, 0xc01d265f, v18
	v_exp_f32_e32 v22, v22
	v_add_f32_e32 v21, v105, v13
	v_med3_f32 v21, v21, s61, v214
	v_add_f32_e32 v22, 1.0, v22
	v_rcp_f32_e32 v22, v22
	s_nop 0
	v_mul_f32_e32 v18, v18, v22
	v_mul_f32_e32 v21, v21, v18
	v_add_f32_e32 v18, v101, v1
	v_min_f32_e32 v18, 0x40e00000, v18
	v_mul_f32_e32 v23, 0xc01d265f, v18
	v_exp_f32_e32 v23, v23
	v_add_f32_e32 v22, v97, v9
	v_med3_f32 v22, v22, s61, v214
	v_add_f32_e32 v23, 1.0, v23
	v_rcp_f32_e32 v23, v23
	s_nop 0
	v_mul_f32_e32 v18, v18, v23
	v_mul_f32_e32 v22, v22, v18
	v_add_f32_e32 v18, v110, v6
	v_min_f32_e32 v18, 0x40e00000, v18
	v_mul_f32_e32 v24, 0xc01d265f, v18
	v_exp_f32_e32 v24, v24
	v_add_f32_e32 v23, v106, v14
	v_med3_f32 v23, v23, s61, v214
	v_add_f32_e32 v24, 1.0, v24
	v_rcp_f32_e32 v24, v24
	s_nop 0
	v_mul_f32_e32 v18, v18, v24
	v_mul_f32_e32 v23, v23, v18
	v_add_f32_e32 v18, v102, v2
	v_min_f32_e32 v18, 0x40e00000, v18
	v_mul_f32_e32 v25, 0xc01d265f, v18
	v_exp_f32_e32 v25, v25
	v_add_f32_e32 v24, v98, v10
	v_med3_f32 v24, v24, s61, v214
	v_add_f32_e32 v25, 1.0, v25
	v_rcp_f32_e32 v25, v25
	s_nop 0
	v_mul_f32_e32 v18, v18, v25
	v_mul_f32_e32 v24, v24, v18
	v_add_f32_e32 v18, v111, v7
	v_min_f32_e32 v18, 0x40e00000, v18
	v_mul_f32_e32 v26, 0xc01d265f, v18
	v_exp_f32_e32 v26, v26
	v_add_f32_e32 v25, v107, v15
	v_med3_f32 v25, v25, s61, v214
	v_add_f32_e32 v26, 1.0, v26
	v_rcp_f32_e32 v26, v26
	s_nop 0
	v_mul_f32_e32 v18, v18, v26
	v_mul_f32_e32 v25, v25, v18
	v_add_f32_e32 v18, v103, v3
	v_min_f32_e32 v18, 0x40e00000, v18
	v_mul_f32_e32 v27, 0xc01d265f, v18
	v_exp_f32_e32 v27, v27
	v_add_f32_e32 v26, v99, v11
	v_med3_f32 v26, v26, s61, v214
	v_add_f32_e32 v27, 1.0, v27
	v_rcp_f32_e32 v27, v27
	s_nop 0
	v_mul_f32_e32 v18, v18, v27
	v_mul_f32_e32 v26, v26, v18
	v_mov_b32_e32 v18, v113
	v_cvt_pk_fp8_f32 v18, v19, v21
	v_mov_b32_e32 v19, v113
	v_cvt_pk_fp8_f32 v19, v20, v22
	v_add_co_u32_e32 v20, vcc, s30, v16
	v_cvt_pk_fp8_f32 v18, v23, v25 op_sel:[0,0,1]
	v_cvt_pk_fp8_f32 v19, v24, v26 op_sel:[0,0,1]
	v_addc_co_u32_e32 v21, vcc, 0, v17, vcc
	global_store_dwordx2 v[20:21], v[18:19], off
	v_add_f32_e32 v18, v92, v4
	v_min_f32_e32 v18, 0x40e00000, v18
	v_mul_f32_e32 v20, 0xc01d265f, v18
	v_exp_f32_e32 v20, v20
	v_add_f32_e32 v19, v88, v12
	v_med3_f32 v19, v19, s61, v214
	v_add_f32_e32 v20, 1.0, v20
	v_rcp_f32_e32 v20, v20
	s_nop 0
	v_mul_f32_e32 v18, v18, v20
	v_mul_f32_e32 v19, v19, v18
	v_add_f32_e32 v18, v84, v0
	v_min_f32_e32 v18, 0x40e00000, v18
	v_mul_f32_e32 v21, 0xc01d265f, v18
	v_exp_f32_e32 v21, v21
	v_add_f32_e32 v20, v80, v8
	v_med3_f32 v20, v20, s61, v214
	v_add_f32_e32 v21, 1.0, v21
	v_rcp_f32_e32 v21, v21
	s_nop 0
	v_mul_f32_e32 v18, v18, v21
	v_mul_f32_e32 v20, v20, v18
	v_add_f32_e32 v18, v93, v5
	v_min_f32_e32 v18, 0x40e00000, v18
	v_mul_f32_e32 v22, 0xc01d265f, v18
	v_exp_f32_e32 v22, v22
	v_add_f32_e32 v21, v89, v13
	v_med3_f32 v21, v21, s61, v214
	v_add_f32_e32 v22, 1.0, v22
	v_rcp_f32_e32 v22, v22
	s_nop 0
	v_mul_f32_e32 v18, v18, v22
	v_mul_f32_e32 v21, v21, v18
	v_add_f32_e32 v18, v85, v1
	v_min_f32_e32 v18, 0x40e00000, v18
	v_mul_f32_e32 v23, 0xc01d265f, v18
	v_exp_f32_e32 v23, v23
	v_add_f32_e32 v22, v81, v9
	v_med3_f32 v22, v22, s61, v214
	v_add_f32_e32 v23, 1.0, v23
	v_rcp_f32_e32 v23, v23
	s_nop 0
	v_mul_f32_e32 v18, v18, v23
	v_mul_f32_e32 v22, v22, v18
	v_add_f32_e32 v18, v94, v6
	v_min_f32_e32 v18, 0x40e00000, v18
	v_mul_f32_e32 v24, 0xc01d265f, v18
	v_exp_f32_e32 v24, v24
	v_add_f32_e32 v23, v90, v14
	v_med3_f32 v23, v23, s61, v214
	v_add_f32_e32 v24, 1.0, v24
	v_rcp_f32_e32 v24, v24
	s_nop 0
	v_mul_f32_e32 v18, v18, v24
	v_mul_f32_e32 v23, v23, v18
	v_add_f32_e32 v18, v86, v2
	v_min_f32_e32 v18, 0x40e00000, v18
	v_mul_f32_e32 v25, 0xc01d265f, v18
	v_exp_f32_e32 v25, v25
	v_add_f32_e32 v24, v82, v10
	v_med3_f32 v24, v24, s61, v214
	v_add_f32_e32 v25, 1.0, v25
	v_rcp_f32_e32 v25, v25
	s_nop 0
	v_mul_f32_e32 v18, v18, v25
	v_mul_f32_e32 v24, v24, v18
	v_add_f32_e32 v18, v95, v7
	v_min_f32_e32 v18, 0x40e00000, v18
	v_mul_f32_e32 v26, 0xc01d265f, v18
	v_exp_f32_e32 v26, v26
	v_add_f32_e32 v25, v91, v15
	v_med3_f32 v25, v25, s61, v214
	v_add_f32_e32 v26, 1.0, v26
	v_rcp_f32_e32 v26, v26
	s_nop 0
	v_mul_f32_e32 v18, v18, v26
	v_mul_f32_e32 v25, v25, v18
	v_add_f32_e32 v18, v87, v3
	v_min_f32_e32 v18, 0x40e00000, v18
	v_mul_f32_e32 v27, 0xc01d265f, v18
	v_exp_f32_e32 v27, v27
	v_add_f32_e32 v26, v83, v11
	v_med3_f32 v26, v26, s61, v214
	v_add_f32_e32 v27, 1.0, v27
	v_rcp_f32_e32 v27, v27
	s_nop 0
	v_mul_f32_e32 v18, v18, v27
	v_mul_f32_e32 v26, v26, v18
	v_mov_b32_e32 v18, v113
	v_cvt_pk_fp8_f32 v18, v19, v21
	v_mov_b32_e32 v19, v113
	v_cvt_pk_fp8_f32 v19, v20, v22
	v_add_co_u32_e32 v20, vcc, s63, v16
	v_cvt_pk_fp8_f32 v18, v23, v25 op_sel:[0,0,1]
	v_cvt_pk_fp8_f32 v19, v24, v26 op_sel:[0,0,1]
	v_addc_co_u32_e32 v21, vcc, 0, v17, vcc
	global_store_dwordx2 v[20:21], v[18:19], off
	v_add_f32_e32 v18, v76, v4
	v_min_f32_e32 v18, 0x40e00000, v18
	v_mul_f32_e32 v20, 0xc01d265f, v18
	v_exp_f32_e32 v20, v20
	v_add_f32_e32 v19, v72, v12
	v_med3_f32 v19, v19, s61, v214
	v_add_f32_e32 v20, 1.0, v20
	v_rcp_f32_e32 v20, v20
	s_nop 0
	v_mul_f32_e32 v18, v18, v20
	v_mul_f32_e32 v19, v19, v18
	v_add_f32_e32 v18, v68, v0
	v_min_f32_e32 v18, 0x40e00000, v18
	v_mul_f32_e32 v21, 0xc01d265f, v18
	v_exp_f32_e32 v21, v21
	v_add_f32_e32 v20, v64, v8
	v_med3_f32 v20, v20, s61, v214
	v_add_f32_e32 v21, 1.0, v21
	v_rcp_f32_e32 v21, v21
	s_nop 0
	v_mul_f32_e32 v18, v18, v21
	v_mul_f32_e32 v20, v20, v18
	v_add_f32_e32 v18, v77, v5
	v_min_f32_e32 v18, 0x40e00000, v18
	v_mul_f32_e32 v22, 0xc01d265f, v18
	v_exp_f32_e32 v22, v22
	v_add_f32_e32 v21, v73, v13
	v_med3_f32 v21, v21, s61, v214
	v_add_f32_e32 v22, 1.0, v22
	v_rcp_f32_e32 v22, v22
	s_nop 0
	v_mul_f32_e32 v18, v18, v22
	v_mul_f32_e32 v21, v21, v18
	v_add_f32_e32 v18, v69, v1
	v_min_f32_e32 v18, 0x40e00000, v18
	v_mul_f32_e32 v23, 0xc01d265f, v18
	v_exp_f32_e32 v23, v23
	v_add_f32_e32 v22, v65, v9
	v_med3_f32 v22, v22, s61, v214
	v_add_f32_e32 v23, 1.0, v23
	v_rcp_f32_e32 v23, v23
	s_nop 0
	v_mul_f32_e32 v18, v18, v23
	v_mul_f32_e32 v22, v22, v18
	v_add_f32_e32 v18, v78, v6
	v_min_f32_e32 v18, 0x40e00000, v18
	v_mul_f32_e32 v24, 0xc01d265f, v18
	v_exp_f32_e32 v24, v24
	v_add_f32_e32 v23, v74, v14
	v_med3_f32 v23, v23, s61, v214
	v_add_f32_e32 v24, 1.0, v24
	v_rcp_f32_e32 v24, v24
	s_nop 0
	v_mul_f32_e32 v18, v18, v24
	v_mul_f32_e32 v23, v23, v18
	v_add_f32_e32 v18, v70, v2
	v_min_f32_e32 v18, 0x40e00000, v18
	v_mul_f32_e32 v25, 0xc01d265f, v18
	v_exp_f32_e32 v25, v25
	v_add_f32_e32 v24, v66, v10
	v_med3_f32 v24, v24, s61, v214
	v_add_f32_e32 v25, 1.0, v25
	v_rcp_f32_e32 v25, v25
	s_nop 0
	v_mul_f32_e32 v18, v18, v25
	v_mul_f32_e32 v24, v24, v18
	v_add_f32_e32 v18, v79, v7
	v_min_f32_e32 v18, 0x40e00000, v18
	v_mul_f32_e32 v26, 0xc01d265f, v18
	v_exp_f32_e32 v26, v26
	v_add_f32_e32 v25, v75, v15
	v_med3_f32 v25, v25, s61, v214
	v_add_f32_e32 v26, 1.0, v26
	v_rcp_f32_e32 v26, v26
	s_nop 0
	v_mul_f32_e32 v18, v18, v26
	v_mul_f32_e32 v25, v25, v18
	v_add_f32_e32 v18, v71, v3
	v_min_f32_e32 v18, 0x40e00000, v18
	v_mul_f32_e32 v27, 0xc01d265f, v18
	v_exp_f32_e32 v27, v27
	v_add_f32_e32 v26, v67, v11
	v_med3_f32 v26, v26, s61, v214
	v_add_f32_e32 v27, 1.0, v27
	v_rcp_f32_e32 v27, v27
	s_nop 0
	v_mul_f32_e32 v18, v18, v27
	v_mul_f32_e32 v26, v26, v18
	v_mov_b32_e32 v18, v113
	v_cvt_pk_fp8_f32 v18, v19, v21
	v_mov_b32_e32 v19, v113
	v_cvt_pk_fp8_f32 v19, v20, v22
	v_add_co_u32_e32 v20, vcc, s21, v16
	v_cvt_pk_fp8_f32 v18, v23, v25 op_sel:[0,0,1]
	v_cvt_pk_fp8_f32 v19, v24, v26 op_sel:[0,0,1]
	v_addc_co_u32_e32 v21, vcc, 0, v17, vcc
	s_mov_b32 s21, 0x28000
	global_store_dwordx2 v[20:21], v[18:19], off
	v_add_f32_e32 v18, v60, v4
	v_min_f32_e32 v18, 0x40e00000, v18
	v_mul_f32_e32 v20, 0xc01d265f, v18
	v_exp_f32_e32 v20, v20
	v_add_f32_e32 v19, v56, v12
	v_med3_f32 v19, v19, s61, v214
	v_add_f32_e32 v4, v44, v4
	v_add_f32_e32 v20, 1.0, v20
	v_rcp_f32_e32 v20, v20
	v_min_f32_e32 v4, 0x40e00000, v4
	v_add_f32_e32 v12, v40, v12
	v_med3_f32 v12, v12, s61, v214
	v_mul_f32_e32 v18, v18, v20
	v_mul_f32_e32 v19, v19, v18
	v_add_f32_e32 v18, v52, v0
	v_min_f32_e32 v18, 0x40e00000, v18
	v_mul_f32_e32 v21, 0xc01d265f, v18
	v_exp_f32_e32 v21, v21
	v_add_f32_e32 v20, v48, v8
	v_med3_f32 v20, v20, s61, v214
	v_add_f32_e32 v0, v36, v0
	v_add_f32_e32 v21, 1.0, v21
	v_rcp_f32_e32 v21, v21
	v_min_f32_e32 v0, 0x40e00000, v0
	v_add_f32_e32 v8, v32, v8
	v_med3_f32 v8, v8, s61, v214
	v_mul_f32_e32 v18, v18, v21
	v_mul_f32_e32 v20, v20, v18
	v_add_f32_e32 v18, v61, v5
	v_min_f32_e32 v18, 0x40e00000, v18
	v_mul_f32_e32 v22, 0xc01d265f, v18
	v_exp_f32_e32 v22, v22
	v_add_f32_e32 v21, v57, v13
	v_med3_f32 v21, v21, s61, v214
	v_add_f32_e32 v22, 1.0, v22
	v_rcp_f32_e32 v22, v22
	s_nop 0
	v_mul_f32_e32 v18, v18, v22
	v_mul_f32_e32 v21, v21, v18
	v_add_f32_e32 v18, v53, v1
	v_min_f32_e32 v18, 0x40e00000, v18
	v_mul_f32_e32 v23, 0xc01d265f, v18
	v_exp_f32_e32 v23, v23
	v_add_f32_e32 v22, v49, v9
	v_med3_f32 v22, v22, s61, v214
	v_add_f32_e32 v23, 1.0, v23
	v_rcp_f32_e32 v23, v23
	s_nop 0
	v_mul_f32_e32 v18, v18, v23
	v_mul_f32_e32 v22, v22, v18
	v_add_f32_e32 v18, v62, v6
	v_min_f32_e32 v18, 0x40e00000, v18
	v_mul_f32_e32 v24, 0xc01d265f, v18
	v_exp_f32_e32 v24, v24
	v_add_f32_e32 v23, v58, v14
	v_med3_f32 v23, v23, s61, v214
	v_add_f32_e32 v24, 1.0, v24
	v_rcp_f32_e32 v24, v24
	s_nop 0
	v_mul_f32_e32 v18, v18, v24
	v_mul_f32_e32 v23, v23, v18
	v_add_f32_e32 v18, v54, v2
	v_min_f32_e32 v18, 0x40e00000, v18
	v_mul_f32_e32 v25, 0xc01d265f, v18
	v_exp_f32_e32 v25, v25
	v_add_f32_e32 v24, v50, v10
	v_med3_f32 v24, v24, s61, v214
	v_add_f32_e32 v25, 1.0, v25
	v_rcp_f32_e32 v25, v25
	s_nop 0
	v_mul_f32_e32 v18, v18, v25
	v_mul_f32_e32 v24, v24, v18
	v_add_f32_e32 v18, v63, v7
	v_min_f32_e32 v18, 0x40e00000, v18
	v_mul_f32_e32 v26, 0xc01d265f, v18
	v_exp_f32_e32 v26, v26
	v_add_f32_e32 v25, v59, v15
	v_med3_f32 v25, v25, s61, v214
	v_add_f32_e32 v26, 1.0, v26
	v_rcp_f32_e32 v26, v26
	s_nop 0
	v_mul_f32_e32 v18, v18, v26
	v_mul_f32_e32 v25, v25, v18
	v_add_f32_e32 v18, v55, v3
	v_min_f32_e32 v18, 0x40e00000, v18
	v_mul_f32_e32 v27, 0xc01d265f, v18
	v_exp_f32_e32 v27, v27
	v_add_f32_e32 v26, v51, v11
	v_med3_f32 v26, v26, s61, v214
	v_add_f32_e32 v27, 1.0, v27
	v_rcp_f32_e32 v27, v27
	s_nop 0
	v_mul_f32_e32 v18, v18, v27
	v_mul_f32_e32 v26, v26, v18
	v_mov_b32_e32 v18, v113
	v_cvt_pk_fp8_f32 v18, v19, v21
	v_mov_b32_e32 v19, v113
	v_cvt_pk_fp8_f32 v19, v20, v22
	v_add_co_u32_e32 v20, vcc, s21, v16
	v_cvt_pk_fp8_f32 v18, v23, v25 op_sel:[0,0,1]
	v_cvt_pk_fp8_f32 v19, v24, v26 op_sel:[0,0,1]
	v_addc_co_u32_e32 v21, vcc, 0, v17, vcc
	s_mov_b32 s21, s20
	global_store_dwordx2 v[20:21], v[18:19], off
	v_mul_f32_e32 v18, 0xc01d265f, v4
	v_exp_f32_e32 v18, v18
	s_nop 0
	v_add_f32_e32 v18, 1.0, v18
	v_rcp_f32_e32 v18, v18
	s_nop 0
	v_mul_f32_e32 v4, v4, v18
	v_mul_f32_e32 v4, v12, v4
	v_mul_f32_e32 v12, 0xc01d265f, v0
	v_exp_f32_e32 v12, v12
	s_nop 0
	v_add_f32_e32 v12, 1.0, v12
	v_rcp_f32_e32 v12, v12
	s_nop 0
	v_mul_f32_e32 v0, v0, v12
	v_mul_f32_e32 v8, v8, v0
	v_add_f32_e32 v0, v45, v5
	v_min_f32_e32 v0, 0x40e00000, v0
	v_mul_f32_e32 v12, 0xc01d265f, v0
	v_exp_f32_e32 v12, v12
	v_add_f32_e32 v5, v41, v13
	v_med3_f32 v5, v5, s61, v214
	v_add_f32_e32 v12, 1.0, v12
	v_rcp_f32_e32 v12, v12
	s_nop 0
	v_mul_f32_e32 v0, v0, v12
	v_mul_f32_e32 v5, v5, v0
	v_add_f32_e32 v0, v37, v1
	v_min_f32_e32 v0, 0x40e00000, v0
	v_add_f32_e32 v1, v33, v9
	v_mul_f32_e32 v9, 0xc01d265f, v0
	v_exp_f32_e32 v9, v9
	v_med3_f32 v1, v1, s61, v214
	v_add_f32_e32 v9, 1.0, v9
	v_rcp_f32_e32 v9, v9
	s_nop 0
	v_mul_f32_e32 v0, v0, v9
	v_mul_f32_e32 v9, v1, v0
	v_add_f32_e32 v0, v46, v6
	v_min_f32_e32 v0, 0x40e00000, v0
	v_mul_f32_e32 v6, 0xc01d265f, v0
	v_exp_f32_e32 v6, v6
	v_add_f32_e32 v1, v42, v14
	v_med3_f32 v1, v1, s61, v214
	v_add_f32_e32 v6, 1.0, v6
	v_rcp_f32_e32 v6, v6
	s_nop 0
	v_mul_f32_e32 v0, v0, v6
	v_mul_f32_e32 v1, v1, v0
	v_add_f32_e32 v0, v38, v2
	v_min_f32_e32 v0, 0x40e00000, v0
	v_mul_f32_e32 v6, 0xc01d265f, v0
	v_exp_f32_e32 v6, v6
	v_add_f32_e32 v2, v34, v10
	v_med3_f32 v2, v2, s61, v214
	v_add_f32_e32 v6, 1.0, v6
	v_rcp_f32_e32 v6, v6
	s_nop 0
	v_mul_f32_e32 v0, v0, v6
	v_mul_f32_e32 v2, v2, v0
	v_add_f32_e32 v0, v47, v7
	v_min_f32_e32 v0, 0x40e00000, v0
	v_mul_f32_e32 v7, 0xc01d265f, v0
	v_exp_f32_e32 v7, v7
	v_add_f32_e32 v6, v43, v15
	v_med3_f32 v6, v6, s61, v214
	v_add_f32_e32 v7, 1.0, v7
	v_rcp_f32_e32 v7, v7
	s_nop 0
	v_mul_f32_e32 v0, v0, v7
	v_mul_f32_e32 v6, v6, v0
	v_add_f32_e32 v0, v39, v3
	v_min_f32_e32 v0, 0x40e00000, v0
	v_mul_f32_e32 v7, 0xc01d265f, v0
	v_exp_f32_e32 v7, v7
	v_add_f32_e32 v3, v35, v11
	v_med3_f32 v3, v3, s61, v214
	v_add_f32_e32 v7, 1.0, v7
	v_rcp_f32_e32 v7, v7
	s_nop 0
	v_mul_f32_e32 v0, v0, v7
	v_mul_f32_e32 v3, v3, v0
	v_mov_b32_e32 v0, v113
	v_cvt_pk_fp8_f32 v0, v4, v5
	v_cvt_pk_fp8_f32 v0, v1, v6 op_sel:[0,0,1]
	v_mov_b32_e32 v1, v113
	v_cvt_pk_fp8_f32 v1, v8, v9
	v_cvt_pk_fp8_f32 v1, v2, v3 op_sel:[0,0,1]
	v_add_co_u32_e32 v2, vcc, 0x2c000, v16
	s_nop 1
	v_addc_co_u32_e32 v3, vcc, 0, v17, vcc
	s_and_b64 vcc, exec, s[38:39]
	global_store_dwordx2 v[2:3], v[0:1], off
	s_cbranch_vccnz .LBB0_1081
	s_andn2_b64 vcc, exec, s[26:27]
	s_cbranch_vccnz .LBB0_1080
	s_barrier
	s_branch .LBB0_1080
